# k_out: gather addresses via v_mad_u32_u16 with op_sel (8 VALU per step instead of 24)
# baseline (speedup 1.0000x reference)
_Z5k_outPKfPK15HIP_vector_typeIiLj2EEPKtS0_S0_Pf:
	v_lshl_or_b32 v6, s2, 8, v0
	v_ashrrev_i32_e32 v2, 3, v6
	s_mov_b32 s2, 0xc350
	v_cmp_gt_i32_e32 vcc, s2, v2
	s_and_saveexec_b64 s[2:3], vcc
	s_cbranch_execz .LBB4_7
	s_load_dwordx4 s[4:7], s[0:1], 0x0
	s_load_dwordx4 s[8:11], s[0:1], 0x18
	v_and_b32_e32 v0, 7, v0
	v_ashrrev_i32_e32 v3, 31, v2
	v_ashrrev_i32_e32 v7, 31, v6
	v_cmp_ne_u32_e32 vcc, 7, v0
	s_waitcnt lgkmcnt(0)
	v_lshl_add_u64 v[4:5], v[2:3], 3, s[6:7]
	v_lshl_add_u64 v[6:7], v[6:7], 2, s[4:5]
	v_cndmask_b32_e32 v1, 0, v0, vcc
	global_load_dwordx2 v[4:5], v[4:5], off
	v_lshlrev_b32_e32 v1, 2, v1
	global_load_dword v8, v[6:7], off
	v_lshl_add_u64 v[6:7], v[2:3], 2, s[8:9]
	global_load_dword v9, v[6:7], off
	global_load_dword v3, v1, s[10:11]
	s_load_dwordx2 s[6:7], s[0:1], 0x28
	s_waitcnt vmcnt(3)
	v_cmp_lt_i32_e64 s[2:3], v4, v5
	s_and_saveexec_b64 s[8:9], s[2:3]
	s_cbranch_execz .LBB4_5
	s_load_dwordx2 s[0:1], s[0:1], 0x10
	v_ashrrev_i32_e32 v7, 31, v4
	v_mov_b32_e32 v6, v4
	v_lshlrev_b32_e32 v1, 2, v0
	s_mov_b64 s[2:3], 0
	s_waitcnt lgkmcnt(0)
	v_lshl_add_u64 v[6:7], v[6:7], 1, s[0:1]
	v_mov_b32_e32 v10, 3
.LBB4_3:
	global_load_dwordx4 v[12:15], v[6:7], off
	v_add_u32_e32 v4, 8, v4
	v_cmp_ge_i32_e64 s[0:1], v4, v5
	v_lshl_add_u64 v[6:7], v[6:7], 0, 16
	s_or_b64 s[2:3], s[0:1], s[2:3]
	s_waitcnt vmcnt(0)
	v_mad_u32_u16 v20, v12, 32, v1
	v_mad_u32_u16 v11, v12, 32, v1 op_sel:[1,0,0,0]
	v_mad_u32_u16 v21, v13, 32, v1
	v_mad_u32_u16 v22, v13, 32, v1 op_sel:[1,0,0,0]
	v_mad_u32_u16 v23, v14, 32, v1
	v_mad_u32_u16 v24, v14, 32, v1 op_sel:[1,0,0,0]
	v_mad_u32_u16 v25, v15, 32, v1
	v_mad_u32_u16 v26, v15, 32, v1 op_sel:[1,0,0,0]
	global_load_dword v12, v20, s[4:5]
	global_load_dword v14, v11, s[4:5]
	global_load_dword v16, v21, s[4:5]
	global_load_dword v18, v22, s[4:5]
	global_load_dword v13, v23, s[4:5]
	global_load_dword v15, v24, s[4:5]
	global_load_dword v17, v25, s[4:5]
	global_load_dword v19, v26, s[4:5]
	s_waitcnt vmcnt(2)
	v_pk_add_f32 v[12:13], v[12:13], v[14:15]
	s_waitcnt vmcnt(0)
	v_pk_add_f32 v[14:15], v[16:17], v[18:19]
	s_nop 0
	v_pk_add_f32 v[12:13], v[12:13], v[14:15]
	s_nop 0
	v_add_f32_e32 v11, v12, v13
	v_add_f32_e32 v8, v8, v11
	s_andn2_b64 exec, exec, s[2:3]
	s_cbranch_execnz .LBB4_3
	s_or_b64 exec, exec, s[2:3]
